# placement: projection GEMM loop at offset 48 mod 64 (others unchanged)
# speedup vs baseline: 1.0033x; 1.0017x over previous
; __device__ __forceinline__ unsigned cvt_pk_bf16(float lo, float hi) { unsigned r; asm volatile("v_cvt_pk_bf16_f32 %0, %1, %2" : "=v"(r) : "v"(lo), "v"(hi)); return r; }
;     __device__ __forceinline__ void operator()(const f32x4 (&acc)[2][2][4][2], const Unit& u, int wr, int wc, int fr, int fq) const {
;     ...
;                 for (int bj = 0; bj < 2; ++bj) { f32x4 v0 = acc[ai][bj][m][0], v1 = acc[ai][bj][m][1]; const int sc = scol0 + bj * HALF;
;                     bf16_t* p;
;                     if (kind == 1) p = Vb + ((size_t)(sc >> 7) * S + row) * HD + (sc & 127);
;                     else if (kind == 2) { p = GBo + (size_t)row * 1024 + sc;
; #pragma unroll
;                         for (int j = 0; j < 4; ++j) { v0[j] = __builtin_amdgcn_rcpf(1.f + __builtin_amdgcn_exp2f(-1.4426950408889634f * v0[j])); v1[j] = __builtin_amdgcn_rcpf(1.f + __builtin_amdgcn_exp2f(-1.4426950408889634f * v1[j])); } }
;                     else p = O + (size_t)row * ldc + u.pn * BM + bj * HALF + wc * 32 + 8 * fq;
;                     u32x4 w; w.x = cvt_pk_bf16(v0[0], v0[1]); w.y = cvt_pk_bf16(v0[2], v0[3]); w.z = cvt_pk_bf16(v1[0], v1[1]); w.w = cvt_pk_bf16(v1[2], v1[3]);
;                     *(u32x4*)p = w; } }
.LBB0_295:
	s_and_b64 vcc, exec, s[14:15]
	s_mov_b32 s57, s56
	s_mov_b32 s4, s12
	s_mov_b64 s[22:23], s[18:19]
	s_mov_b64 s[20:21], s[16:17]
	v_cvt_pk_bf16_f32 v2, v12, v14
	v_cvt_pk_bf16_f32 v3, v16, v24
	v_cvt_pk_bf16_f32 v4, v13, v15
	v_cvt_pk_bf16_f32 v5, v17, v19
	global_store_dwordx4 v[10:11], v[2:5], off
	s_cbranch_vccnz .LBB0_433
	s_nop 0
	s_nop 0
	s_nop 0
	s_nop 0
	s_nop 0
	s_nop 0
	s_nop 0
	s_nop 0

; __device__ __forceinline__ unsigned cvt_pk_bf16(float lo, float hi) { unsigned r; asm volatile("v_cvt_pk_bf16_f32 %0, %1, %2" : "=v"(r) : "v"(lo), "v"(hi)); return r; }
; __global__ void __launch_bounds__(NTHREADS, 2) mega_fwd(Args args) {
;     ...
;             for (int i = 0; i < 16; ++i) { const double cs = (base + loc[i]) * 11.313708498984761;
;                 const unsigned b1 = cvt_pk_bf16((float)cs, 0.f) & 0xffffu; const double r1 = cs - (double)__uint_as_float(b1 << 16);
;                 const unsigned b2 = cvt_pk_bf16((float)r1, 0.f) & 0xffffu; const double r2 = r1 - (double)__uint_as_float(b2 << 16);
;                 const unsigned b3 = cvt_pk_bf16((float)r2, 0.f) & 0xffffu; const unsigned one = 0x3f80u;
;                 const size_t e = ((size_t)h * S + tid * 16 + i) * 8;
;                 *(u32x4*)(QX + e) = (u32x4){b1 | (b2 << 16), b3 | (one << 16), one | (one << 16), 0u};
;                 *(u32x4*)(KX + e) = (u32x4){one | (one << 16), one | ((b1 ^ 0x8000u) << 16), (b2 ^ 0x8000u) | ((b3 ^ 0x8000u) << 16), 0u}; }
.LBB0_642:
	s_or_b64 exec, exec, s[8:9]
	s_mov_b32 s12, 0x667f3bcd
	s_mov_b32 s13, 0x4026a09e
	v_mul_f64 v[2:3], v[50:51], s[12:13]
	v_cvt_f32_f64_e32 v2, v[2:3]
	v_mov_b32_e32 v4, 0
	v_cvt_pk_bf16_f32 v5, v2, v4
	v_readlane_b32 s0, v241, 5
	v_lshlrev_b32_e32 v12, 16, v5
	v_cvt_f64_f32_e32 v[2:3], v12
	v_fma_f64 v[2:3], v[50:51], s[12:13], -v[2:3]
	v_cvt_f32_f64_e32 v6, v[2:3]
	v_readlane_b32 s1, v241, 6
	s_add_u32 s10, s0, 0x400000
	v_cvt_pk_bf16_f32 v6, v6, v4
	s_addc_u32 s11, s1, 0
	v_lshlrev_b32_e32 v8, 16, v6
	v_and_b32_e32 v13, 0xffff, v6
	v_cvt_f64_f32_e32 v[6:7], v8
	s_add_u32 s8, s0, 0x500000
	v_add_f64 v[2:3], v[2:3], -v[6:7]
	s_addc_u32 s9, s1, 0
	s_mov_b32 s3, 0
	s_mov_b32 s1, 0xffff
	v_cvt_f32_f64_e32 v2, v[2:3]
	s_mov_b32 s2, 0x3f803f80
	v_cvt_pk_bf16_f32 v14, v2, v4
	v_and_or_b32 v2, v5, s1, v8
	v_mov_b64_e32 v[8:9], s[2:3]
	v_and_or_b32 v3, v14, s1, 1.0
	v_mov_b64_e32 v[6:7], s[0:1]
	s_lshl_b64 s[6:7], s[6:7], 17
	v_mov_b32_e32 v6, v2
	v_mov_b32_e32 v7, v3
	v_lshl_or_b32 v2, v1, 4, s6
	v_mov_b32_e32 v3, s7
	v_lshl_add_u64 v[10:11], s[10:11], 0, v[2:3]
	global_store_dwordx4 v[10:11], v[6:9], off
	v_lshlrev_b32_e32 v5, 16, v14
	s_mov_b32 s6, 0x80008000
	s_mov_b32 s0, s2
	v_mov_b64_e32 v[8:9], s[2:3]
	v_xor_b32_e32 v1, 0x80003f80, v12
	v_bitop3_b32 v5, v5, s6, v13 bitop3:0x36
	v_mov_b64_e32 v[6:7], s[0:1]
	v_mov_b32_e32 v7, v1
	v_mov_b32_e32 v8, v5
	v_lshl_add_u64 v[10:11], s[8:9], 0, v[2:3]
	global_store_dwordx4 v[10:11], v[6:9], off
	v_mov_b32_e32 v11, s7
	s_nop 0
	v_mul_f64 v[6:7], v[48:49], s[12:13]
	v_cvt_f32_f64_e32 v1, v[6:7]
	v_cvt_pk_bf16_f32 v1, v1, v4
	s_nop 0
	v_lshlrev_b32_e32 v5, 16, v1
	v_cvt_f64_f32_e32 v[6:7], v5
	v_fma_f64 v[6:7], v[48:49], s[12:13], -v[6:7]
	v_cvt_f32_f64_e32 v8, v[6:7]
	v_cvt_pk_bf16_f32 v8, v8, v4
	s_nop 0
	v_lshlrev_b32_e32 v10, 16, v8
	v_and_b32_e32 v14, 0xffff, v8
	v_cvt_f64_f32_e32 v[8:9], v10
	v_add_f64 v[6:7], v[6:7], -v[8:9]
	v_cvt_f32_f64_e32 v6, v[6:7]
	v_cvt_pk_bf16_f32 v15, v6, v4
	v_mov_b64_e32 v[8:9], s[2:3]
	v_and_or_b32 v1, v1, s1, v10
	v_and_or_b32 v10, v15, s1, 1.0
	v_mov_b64_e32 v[6:7], s[0:1]
	v_mov_b32_e32 v7, v10
	v_or_b32_e32 v10, 16, v2
	v_mov_b32_e32 v6, v1
	v_lshl_add_u64 v[12:13], s[10:11], 0, v[10:11]
	global_store_dwordx4 v[12:13], v[6:9], off
	v_xor_b32_e32 v1, 0x80003f80, v5
	v_lshlrev_b32_e32 v5, 16, v15
	v_mov_b64_e32 v[8:9], s[2:3]
	v_bitop3_b32 v5, v5, s6, v14 bitop3:0x36
	v_mov_b64_e32 v[6:7], s[0:1]
	v_mov_b32_e32 v7, v1
	v_mov_b32_e32 v8, v5
	v_lshl_add_u64 v[10:11], s[8:9], 0, v[10:11]
	global_store_dwordx4 v[10:11], v[6:9], off
	v_mov_b32_e32 v11, s7
	s_nop 0
	v_mul_f64 v[6:7], v[46:47], s[12:13]
	v_cvt_f32_f64_e32 v1, v[6:7]
	v_cvt_pk_bf16_f32 v1, v1, v4
	s_nop 0
	v_lshlrev_b32_e32 v5, 16, v1
	v_cvt_f64_f32_e32 v[6:7], v5
	v_fma_f64 v[6:7], v[46:47], s[12:13], -v[6:7]
	v_cvt_f32_f64_e32 v8, v[6:7]
	v_cvt_pk_bf16_f32 v8, v8, v4
	s_nop 0
	v_lshlrev_b32_e32 v10, 16, v8
	v_and_b32_e32 v14, 0xffff, v8
	v_cvt_f64_f32_e32 v[8:9], v10
	v_add_f64 v[6:7], v[6:7], -v[8:9]
	v_cvt_f32_f64_e32 v6, v[6:7]
	v_cvt_pk_bf16_f32 v15, v6, v4
	v_mov_b64_e32 v[8:9], s[2:3]
	v_and_or_b32 v1, v1, s1, v10
	v_and_or_b32 v10, v15, s1, 1.0
	v_mov_b64_e32 v[6:7], s[0:1]
	v_mov_b32_e32 v7, v10
	v_or_b32_e32 v10, 32, v2
	v_mov_b32_e32 v6, v1
	v_lshl_add_u64 v[12:13], s[10:11], 0, v[10:11]
	global_store_dwordx4 v[12:13], v[6:9], off
	v_xor_b32_e32 v1, 0x80003f80, v5
	v_lshlrev_b32_e32 v5, 16, v15
	v_mov_b64_e32 v[8:9], s[2:3]
	v_bitop3_b32 v5, v5, s6, v14 bitop3:0x36
	v_mov_b64_e32 v[6:7], s[0:1]
	v_mov_b32_e32 v7, v1
	v_mov_b32_e32 v8, v5
	v_lshl_add_u64 v[10:11], s[8:9], 0, v[10:11]
	global_store_dwordx4 v[10:11], v[6:9], off
	v_mov_b32_e32 v11, s7
	s_nop 0
	v_mul_f64 v[6:7], v[44:45], s[12:13]
	v_cvt_f32_f64_e32 v1, v[6:7]
	v_cvt_pk_bf16_f32 v1, v1, v4
	s_nop 0
	v_lshlrev_b32_e32 v5, 16, v1
	v_cvt_f64_f32_e32 v[6:7], v5
	v_fma_f64 v[6:7], v[44:45], s[12:13], -v[6:7]
	v_cvt_f32_f64_e32 v8, v[6:7]
	v_cvt_pk_bf16_f32 v8, v8, v4
	s_nop 0
	v_lshlrev_b32_e32 v10, 16, v8
	v_and_b32_e32 v14, 0xffff, v8
	v_cvt_f64_f32_e32 v[8:9], v10
	v_add_f64 v[6:7], v[6:7], -v[8:9]
	v_cvt_f32_f64_e32 v6, v[6:7]
	v_cvt_pk_bf16_f32 v15, v6, v4
	v_mov_b64_e32 v[8:9], s[2:3]
	v_and_or_b32 v1, v1, s1, v10
	v_and_or_b32 v10, v15, s1, 1.0
	v_mov_b64_e32 v[6:7], s[0:1]
	v_mov_b32_e32 v7, v10
	v_or_b32_e32 v10, 48, v2
	v_mov_b32_e32 v6, v1
	v_lshl_add_u64 v[12:13], s[10:11], 0, v[10:11]
	global_store_dwordx4 v[12:13], v[6:9], off
	v_xor_b32_e32 v1, 0x80003f80, v5
	v_lshlrev_b32_e32 v5, 16, v15
	v_mov_b64_e32 v[8:9], s[2:3]
	v_bitop3_b32 v5, v5, s6, v14 bitop3:0x36
	v_mov_b64_e32 v[6:7], s[0:1]
	v_mov_b32_e32 v7, v1
	v_mov_b32_e32 v8, v5
	v_lshl_add_u64 v[10:11], s[8:9], 0, v[10:11]
	global_store_dwordx4 v[10:11], v[6:9], off
	v_mov_b32_e32 v11, s7
	s_nop 0
	v_mul_f64 v[6:7], v[42:43], s[12:13]
	v_cvt_f32_f64_e32 v1, v[6:7]
	v_cvt_pk_bf16_f32 v1, v1, v4
	s_nop 0
	v_lshlrev_b32_e32 v5, 16, v1
	v_cvt_f64_f32_e32 v[6:7], v5
	v_fma_f64 v[6:7], v[42:43], s[12:13], -v[6:7]
	v_cvt_f32_f64_e32 v8, v[6:7]
	v_cvt_pk_bf16_f32 v8, v8, v4
	s_nop 0
	v_lshlrev_b32_e32 v10, 16, v8
	v_and_b32_e32 v14, 0xffff, v8
	v_cvt_f64_f32_e32 v[8:9], v10
	v_add_f64 v[6:7], v[6:7], -v[8:9]
	v_cvt_f32_f64_e32 v6, v[6:7]
	v_cvt_pk_bf16_f32 v15, v6, v4
	v_mov_b64_e32 v[8:9], s[2:3]
	v_and_or_b32 v1, v1, s1, v10
	v_and_or_b32 v10, v15, s1, 1.0
	v_mov_b64_e32 v[6:7], s[0:1]
	v_mov_b32_e32 v7, v10
	v_or_b32_e32 v10, 64, v2
	v_mov_b32_e32 v6, v1
	v_lshl_add_u64 v[12:13], s[10:11], 0, v[10:11]
	global_store_dwordx4 v[12:13], v[6:9], off
	v_xor_b32_e32 v1, 0x80003f80, v5
	v_lshlrev_b32_e32 v5, 16, v15
	v_mov_b64_e32 v[8:9], s[2:3]
; __device__ __forceinline__ unsigned cvt_pk_bf16(float lo, float hi) { unsigned r; asm volatile("v_cvt_pk_bf16_f32 %0, %1, %2" : "=v"(r) : "v"(lo), "v"(hi)); return r; }
; __global__ void __launch_bounds__(NTHREADS, 2) mega_fwd(Args args) {
;     ...
;             for (int i = 0; i < 16; ++i) { const double cs = (base + loc[i]) * 11.313708498984761;
;                 const unsigned b1 = cvt_pk_bf16((float)cs, 0.f) & 0xffffu; const double r1 = cs - (double)__uint_as_float(b1 << 16);
;                 const unsigned b2 = cvt_pk_bf16((float)r1, 0.f) & 0xffffu; const double r2 = r1 - (double)__uint_as_float(b2 << 16);
;                 const unsigned b3 = cvt_pk_bf16((float)r2, 0.f) & 0xffffu; const unsigned one = 0x3f80u;
;                 const size_t e = ((size_t)h * S + tid * 16 + i) * 8;
;                 *(u32x4*)(QX + e) = (u32x4){b1 | (b2 << 16), b3 | (one << 16), one | (one << 16), 0u};
;                 *(u32x4*)(KX + e) = (u32x4){one | (one << 16), one | ((b1 ^ 0x8000u) << 16), (b2 ^ 0x8000u) | ((b3 ^ 0x8000u) << 16), 0u}; }
	v_bitop3_b32 v5, v5, s6, v14 bitop3:0x36
	v_mov_b64_e32 v[6:7], s[0:1]
	v_mov_b32_e32 v7, v1
	v_mov_b32_e32 v8, v5
	v_lshl_add_u64 v[10:11], s[8:9], 0, v[10:11]
	global_store_dwordx4 v[10:11], v[6:9], off
	v_mov_b32_e32 v11, s7
	s_nop 0
	v_mul_f64 v[6:7], v[40:41], s[12:13]
	v_cvt_f32_f64_e32 v1, v[6:7]
	v_cvt_pk_bf16_f32 v1, v1, v4
	s_nop 0
	v_lshlrev_b32_e32 v5, 16, v1
	v_cvt_f64_f32_e32 v[6:7], v5
	v_fma_f64 v[6:7], v[40:41], s[12:13], -v[6:7]
	v_cvt_f32_f64_e32 v8, v[6:7]
	v_cvt_pk_bf16_f32 v8, v8, v4
	s_nop 0
	v_lshlrev_b32_e32 v10, 16, v8
	v_and_b32_e32 v14, 0xffff, v8
	v_cvt_f64_f32_e32 v[8:9], v10
	v_add_f64 v[6:7], v[6:7], -v[8:9]
	v_cvt_f32_f64_e32 v6, v[6:7]
	v_cvt_pk_bf16_f32 v15, v6, v4
	v_mov_b64_e32 v[8:9], s[2:3]
	v_and_or_b32 v1, v1, s1, v10
	v_and_or_b32 v10, v15, s1, 1.0
	v_mov_b64_e32 v[6:7], s[0:1]
	v_mov_b32_e32 v7, v10
	v_or_b32_e32 v10, 0x50, v2
	v_mov_b32_e32 v6, v1
	v_lshl_add_u64 v[12:13], s[10:11], 0, v[10:11]
	global_store_dwordx4 v[12:13], v[6:9], off
	v_xor_b32_e32 v1, 0x80003f80, v5
	v_lshlrev_b32_e32 v5, 16, v15
	v_mov_b64_e32 v[8:9], s[2:3]
	v_bitop3_b32 v5, v5, s6, v14 bitop3:0x36
	v_mov_b64_e32 v[6:7], s[0:1]
	v_mov_b32_e32 v7, v1
	v_mov_b32_e32 v8, v5
	v_lshl_add_u64 v[10:11], s[8:9], 0, v[10:11]
	global_store_dwordx4 v[10:11], v[6:9], off
	v_mov_b32_e32 v11, s7
	s_nop 0
	v_mul_f64 v[6:7], v[38:39], s[12:13]
	v_cvt_f32_f64_e32 v1, v[6:7]
	v_cvt_pk_bf16_f32 v1, v1, v4
	s_nop 0
	v_lshlrev_b32_e32 v5, 16, v1
	v_cvt_f64_f32_e32 v[6:7], v5
	v_fma_f64 v[6:7], v[38:39], s[12:13], -v[6:7]
	v_cvt_f32_f64_e32 v8, v[6:7]
	v_cvt_pk_bf16_f32 v8, v8, v4
	s_nop 0
	v_lshlrev_b32_e32 v10, 16, v8
	v_and_b32_e32 v14, 0xffff, v8
	v_cvt_f64_f32_e32 v[8:9], v10
	v_add_f64 v[6:7], v[6:7], -v[8:9]
	v_cvt_f32_f64_e32 v6, v[6:7]
	v_cvt_pk_bf16_f32 v15, v6, v4
	v_mov_b64_e32 v[8:9], s[2:3]
	v_and_or_b32 v1, v1, s1, v10
	v_and_or_b32 v10, v15, s1, 1.0
	v_mov_b64_e32 v[6:7], s[0:1]
	v_mov_b32_e32 v7, v10
	v_or_b32_e32 v10, 0x60, v2
	v_mov_b32_e32 v6, v1
	v_lshl_add_u64 v[12:13], s[10:11], 0, v[10:11]
	global_store_dwordx4 v[12:13], v[6:9], off
	v_xor_b32_e32 v1, 0x80003f80, v5
	v_lshlrev_b32_e32 v5, 16, v15
	v_mov_b64_e32 v[8:9], s[2:3]
	v_bitop3_b32 v5, v5, s6, v14 bitop3:0x36
	v_mov_b64_e32 v[6:7], s[0:1]
	v_mov_b32_e32 v7, v1
	v_mov_b32_e32 v8, v5
	v_lshl_add_u64 v[10:11], s[8:9], 0, v[10:11]
	global_store_dwordx4 v[10:11], v[6:9], off
	v_mov_b32_e32 v11, s7
	s_nop 0
	v_mul_f64 v[6:7], v[36:37], s[12:13]
	v_cvt_f32_f64_e32 v1, v[6:7]
	v_cvt_pk_bf16_f32 v1, v1, v4
	s_nop 0
	v_lshlrev_b32_e32 v5, 16, v1
	v_cvt_f64_f32_e32 v[6:7], v5
	v_fma_f64 v[6:7], v[36:37], s[12:13], -v[6:7]
	v_cvt_f32_f64_e32 v8, v[6:7]
	v_cvt_pk_bf16_f32 v8, v8, v4
	s_nop 0
	v_lshlrev_b32_e32 v10, 16, v8
	v_and_b32_e32 v14, 0xffff, v8
	v_cvt_f64_f32_e32 v[8:9], v10
	v_add_f64 v[6:7], v[6:7], -v[8:9]
	v_cvt_f32_f64_e32 v6, v[6:7]
	v_cvt_pk_bf16_f32 v15, v6, v4
	v_mov_b64_e32 v[8:9], s[2:3]
	v_and_or_b32 v1, v1, s1, v10
	v_and_or_b32 v10, v15, s1, 1.0
	v_mov_b64_e32 v[6:7], s[0:1]
	v_mov_b32_e32 v7, v10
	v_or_b32_e32 v10, 0x70, v2
	v_mov_b32_e32 v6, v1
	v_lshl_add_u64 v[12:13], s[10:11], 0, v[10:11]
	global_store_dwordx4 v[12:13], v[6:9], off
	v_xor_b32_e32 v1, 0x80003f80, v5
	v_lshlrev_b32_e32 v5, 16, v15
	v_mov_b64_e32 v[8:9], s[2:3]
	v_bitop3_b32 v5, v5, s6, v14 bitop3:0x36
	v_mov_b64_e32 v[6:7], s[0:1]
	v_mov_b32_e32 v7, v1
	v_mov_b32_e32 v8, v5
	v_lshl_add_u64 v[10:11], s[8:9], 0, v[10:11]
	global_store_dwordx4 v[10:11], v[6:9], off
	v_mov_b32_e32 v11, s7
	s_nop 0
	v_mul_f64 v[6:7], v[34:35], s[12:13]
	v_cvt_f32_f64_e32 v1, v[6:7]
	v_cvt_pk_bf16_f32 v1, v1, v4
	s_nop 0
	v_lshlrev_b32_e32 v5, 16, v1
	v_cvt_f64_f32_e32 v[6:7], v5
	v_fma_f64 v[6:7], v[34:35], s[12:13], -v[6:7]
	v_cvt_f32_f64_e32 v8, v[6:7]
	v_cvt_pk_bf16_f32 v8, v8, v4
	s_nop 0
	v_lshlrev_b32_e32 v10, 16, v8
	v_and_b32_e32 v14, 0xffff, v8
	v_cvt_f64_f32_e32 v[8:9], v10
	v_add_f64 v[6:7], v[6:7], -v[8:9]
	v_cvt_f32_f64_e32 v6, v[6:7]
	v_cvt_pk_bf16_f32 v15, v6, v4
	v_mov_b64_e32 v[8:9], s[2:3]
	v_and_or_b32 v1, v1, s1, v10
	v_and_or_b32 v10, v15, s1, 1.0
	v_mov_b64_e32 v[6:7], s[0:1]
	v_mov_b32_e32 v7, v10
	v_or_b32_e32 v10, 0x80, v2
	v_mov_b32_e32 v6, v1
	v_lshl_add_u64 v[12:13], s[10:11], 0, v[10:11]
	global_store_dwordx4 v[12:13], v[6:9], off
	v_xor_b32_e32 v1, 0x80003f80, v5
	v_lshlrev_b32_e32 v5, 16, v15
	v_mov_b64_e32 v[8:9], s[2:3]
	v_bitop3_b32 v5, v5, s6, v14 bitop3:0x36
	v_mov_b64_e32 v[6:7], s[0:1]
	v_mov_b32_e32 v7, v1
	v_mov_b32_e32 v8, v5
	v_lshl_add_u64 v[10:11], s[8:9], 0, v[10:11]
	global_store_dwordx4 v[10:11], v[6:9], off
	v_mov_b32_e32 v11, s7
	s_nop 0
	v_mul_f64 v[6:7], v[32:33], s[12:13]
	v_cvt_f32_f64_e32 v1, v[6:7]
	v_cvt_pk_bf16_f32 v1, v1, v4
	s_nop 0
	v_lshlrev_b32_e32 v5, 16, v1
	v_cvt_f64_f32_e32 v[6:7], v5
	v_fma_f64 v[6:7], v[32:33], s[12:13], -v[6:7]
	v_cvt_f32_f64_e32 v8, v[6:7]
	v_cvt_pk_bf16_f32 v8, v8, v4
	s_nop 0
	v_lshlrev_b32_e32 v10, 16, v8
	v_and_b32_e32 v14, 0xffff, v8
	v_cvt_f64_f32_e32 v[8:9], v10
	v_add_f64 v[6:7], v[6:7], -v[8:9]
	v_cvt_f32_f64_e32 v6, v[6:7]
	v_cvt_pk_bf16_f32 v15, v6, v4
	v_mov_b64_e32 v[8:9], s[2:3]
	v_and_or_b32 v1, v1, s1, v10
	v_and_or_b32 v10, v15, s1, 1.0
	v_mov_b64_e32 v[6:7], s[0:1]
	v_mov_b32_e32 v7, v10
	v_or_b32_e32 v10, 0x90, v2
	v_mov_b32_e32 v6, v1
	v_lshl_add_u64 v[12:13], s[10:11], 0, v[10:11]
	global_store_dwordx4 v[12:13], v[6:9], off
	v_xor_b32_e32 v1, 0x80003f80, v5
	v_lshlrev_b32_e32 v5, 16, v15
	v_mov_b64_e32 v[8:9], s[2:3]
	v_bitop3_b32 v5, v5, s6, v14 bitop3:0x36
	v_mov_b64_e32 v[6:7], s[0:1]
	v_mov_b32_e32 v7, v1
	v_mov_b32_e32 v8, v5
	v_lshl_add_u64 v[10:11], s[8:9], 0, v[10:11]
; __device__ __forceinline__ unsigned cvt_pk_bf16(float lo, float hi) { unsigned r; asm volatile("v_cvt_pk_bf16_f32 %0, %1, %2" : "=v"(r) : "v"(lo), "v"(hi)); return r; }
; __global__ void __launch_bounds__(NTHREADS, 2) mega_fwd(Args args) {
;     ...
;             for (int i = 0; i < 16; ++i) { const double cs = (base + loc[i]) * 11.313708498984761;
;                 const unsigned b1 = cvt_pk_bf16((float)cs, 0.f) & 0xffffu; const double r1 = cs - (double)__uint_as_float(b1 << 16);
;                 const unsigned b2 = cvt_pk_bf16((float)r1, 0.f) & 0xffffu; const double r2 = r1 - (double)__uint_as_float(b2 << 16);
;                 const unsigned b3 = cvt_pk_bf16((float)r2, 0.f) & 0xffffu; const unsigned one = 0x3f80u;
;                 const size_t e = ((size_t)h * S + tid * 16 + i) * 8;
;                 *(u32x4*)(QX + e) = (u32x4){b1 | (b2 << 16), b3 | (one << 16), one | (one << 16), 0u};
;                 *(u32x4*)(KX + e) = (u32x4){one | (one << 16), one | ((b1 ^ 0x8000u) << 16), (b2 ^ 0x8000u) | ((b3 ^ 0x8000u) << 16), 0u}; }
	global_store_dwordx4 v[10:11], v[6:9], off
	v_mov_b32_e32 v11, s7
	s_nop 0
	v_mul_f64 v[6:7], v[30:31], s[12:13]
	v_cvt_f32_f64_e32 v1, v[6:7]
	v_cvt_pk_bf16_f32 v1, v1, v4
	s_nop 0
	v_lshlrev_b32_e32 v5, 16, v1
	v_cvt_f64_f32_e32 v[6:7], v5
	v_fma_f64 v[6:7], v[30:31], s[12:13], -v[6:7]
	v_cvt_f32_f64_e32 v8, v[6:7]
	v_cvt_pk_bf16_f32 v8, v8, v4
	s_nop 0
	v_lshlrev_b32_e32 v10, 16, v8
	v_and_b32_e32 v14, 0xffff, v8
	v_cvt_f64_f32_e32 v[8:9], v10
	v_add_f64 v[6:7], v[6:7], -v[8:9]
	v_cvt_f32_f64_e32 v6, v[6:7]
	v_cvt_pk_bf16_f32 v15, v6, v4
	v_mov_b64_e32 v[8:9], s[2:3]
	v_and_or_b32 v1, v1, s1, v10
	v_and_or_b32 v10, v15, s1, 1.0
	v_mov_b64_e32 v[6:7], s[0:1]
	v_mov_b32_e32 v7, v10
	v_or_b32_e32 v10, 0xa0, v2
	v_mov_b32_e32 v6, v1
	v_lshl_add_u64 v[12:13], s[10:11], 0, v[10:11]
	global_store_dwordx4 v[12:13], v[6:9], off
	v_xor_b32_e32 v1, 0x80003f80, v5
	v_lshlrev_b32_e32 v5, 16, v15
	v_mov_b64_e32 v[8:9], s[2:3]
	v_bitop3_b32 v5, v5, s6, v14 bitop3:0x36
	v_mov_b64_e32 v[6:7], s[0:1]
	v_mov_b32_e32 v7, v1
	v_mov_b32_e32 v8, v5
	v_lshl_add_u64 v[10:11], s[8:9], 0, v[10:11]
	global_store_dwordx4 v[10:11], v[6:9], off
	v_mov_b32_e32 v11, s7
	s_nop 0
	v_mul_f64 v[6:7], v[28:29], s[12:13]
	v_cvt_f32_f64_e32 v1, v[6:7]
	v_cvt_pk_bf16_f32 v1, v1, v4
	s_nop 0
	v_lshlrev_b32_e32 v5, 16, v1
	v_cvt_f64_f32_e32 v[6:7], v5
	v_fma_f64 v[6:7], v[28:29], s[12:13], -v[6:7]
	v_cvt_f32_f64_e32 v8, v[6:7]
	v_cvt_pk_bf16_f32 v8, v8, v4
	s_nop 0
	v_lshlrev_b32_e32 v10, 16, v8
	v_and_b32_e32 v14, 0xffff, v8
	v_cvt_f64_f32_e32 v[8:9], v10
	v_add_f64 v[6:7], v[6:7], -v[8:9]
	v_cvt_f32_f64_e32 v6, v[6:7]
	v_cvt_pk_bf16_f32 v15, v6, v4
	v_mov_b64_e32 v[8:9], s[2:3]
	v_and_or_b32 v1, v1, s1, v10
	v_and_or_b32 v10, v15, s1, 1.0
	v_mov_b64_e32 v[6:7], s[0:1]
	v_mov_b32_e32 v7, v10
	v_or_b32_e32 v10, 0xb0, v2
	v_mov_b32_e32 v6, v1
	v_lshl_add_u64 v[12:13], s[10:11], 0, v[10:11]
	global_store_dwordx4 v[12:13], v[6:9], off
	v_xor_b32_e32 v1, 0x80003f80, v5
	v_lshlrev_b32_e32 v5, 16, v15
	v_mov_b64_e32 v[8:9], s[2:3]
	v_bitop3_b32 v5, v5, s6, v14 bitop3:0x36
	v_mov_b64_e32 v[6:7], s[0:1]
	v_mov_b32_e32 v7, v1
	v_mov_b32_e32 v8, v5
	v_lshl_add_u64 v[10:11], s[8:9], 0, v[10:11]
	global_store_dwordx4 v[10:11], v[6:9], off
	v_mov_b32_e32 v11, s7
	s_nop 0
	v_mul_f64 v[6:7], v[26:27], s[12:13]
	v_cvt_f32_f64_e32 v1, v[6:7]
	v_cvt_pk_bf16_f32 v1, v1, v4
	s_nop 0
	v_lshlrev_b32_e32 v5, 16, v1
	v_cvt_f64_f32_e32 v[6:7], v5
	v_fma_f64 v[6:7], v[26:27], s[12:13], -v[6:7]
	v_cvt_f32_f64_e32 v8, v[6:7]
	v_cvt_pk_bf16_f32 v8, v8, v4
	s_nop 0
	v_lshlrev_b32_e32 v10, 16, v8
	v_and_b32_e32 v14, 0xffff, v8
	v_cvt_f64_f32_e32 v[8:9], v10
	v_add_f64 v[6:7], v[6:7], -v[8:9]
	v_cvt_f32_f64_e32 v6, v[6:7]
	v_cvt_pk_bf16_f32 v15, v6, v4
	v_mov_b64_e32 v[8:9], s[2:3]
	v_and_or_b32 v1, v1, s1, v10
	v_and_or_b32 v10, v15, s1, 1.0
	v_mov_b64_e32 v[6:7], s[0:1]
	v_mov_b32_e32 v7, v10
	v_or_b32_e32 v10, 0xc0, v2
	v_mov_b32_e32 v6, v1
	v_lshl_add_u64 v[12:13], s[10:11], 0, v[10:11]
	global_store_dwordx4 v[12:13], v[6:9], off
	v_xor_b32_e32 v1, 0x80003f80, v5
	v_lshlrev_b32_e32 v5, 16, v15
	v_mov_b64_e32 v[8:9], s[2:3]
	v_bitop3_b32 v5, v5, s6, v14 bitop3:0x36
	v_mov_b64_e32 v[6:7], s[0:1]
	v_mov_b32_e32 v7, v1
	v_mov_b32_e32 v8, v5
	v_lshl_add_u64 v[10:11], s[8:9], 0, v[10:11]
	global_store_dwordx4 v[10:11], v[6:9], off
	v_mov_b32_e32 v11, s7
	s_nop 0
	v_mul_f64 v[6:7], v[24:25], s[12:13]
	v_cvt_f32_f64_e32 v1, v[6:7]
	v_cvt_pk_bf16_f32 v1, v1, v4
	s_nop 0
	v_lshlrev_b32_e32 v5, 16, v1
	v_cvt_f64_f32_e32 v[6:7], v5
	v_fma_f64 v[6:7], v[24:25], s[12:13], -v[6:7]
	v_cvt_f32_f64_e32 v8, v[6:7]
	v_cvt_pk_bf16_f32 v8, v8, v4
	s_nop 0
	v_lshlrev_b32_e32 v10, 16, v8
	v_and_b32_e32 v14, 0xffff, v8
	v_cvt_f64_f32_e32 v[8:9], v10
	v_add_f64 v[6:7], v[6:7], -v[8:9]
	v_cvt_f32_f64_e32 v6, v[6:7]
	v_cvt_pk_bf16_f32 v15, v6, v4
	v_mov_b64_e32 v[8:9], s[2:3]
	v_and_or_b32 v1, v1, s1, v10
	v_and_or_b32 v10, v15, s1, 1.0
	v_mov_b64_e32 v[6:7], s[0:1]
	v_mov_b32_e32 v7, v10
	v_or_b32_e32 v10, 0xd0, v2
	v_mov_b32_e32 v6, v1
	v_lshl_add_u64 v[12:13], s[10:11], 0, v[10:11]
	global_store_dwordx4 v[12:13], v[6:9], off
	v_xor_b32_e32 v1, 0x80003f80, v5
	v_lshlrev_b32_e32 v5, 16, v15
	v_mov_b64_e32 v[8:9], s[2:3]
	v_bitop3_b32 v5, v5, s6, v14 bitop3:0x36
	v_mov_b64_e32 v[6:7], s[0:1]
	v_mov_b32_e32 v7, v1
	v_mov_b32_e32 v8, v5
	v_lshl_add_u64 v[10:11], s[8:9], 0, v[10:11]
	global_store_dwordx4 v[10:11], v[6:9], off
	v_mov_b32_e32 v11, s7
	s_nop 0
	v_mul_f64 v[6:7], v[22:23], s[12:13]
	v_cvt_f32_f64_e32 v1, v[6:7]
	v_cvt_pk_bf16_f32 v1, v1, v4
	s_nop 0
	v_lshlrev_b32_e32 v5, 16, v1
	v_cvt_f64_f32_e32 v[6:7], v5
	v_fma_f64 v[6:7], v[22:23], s[12:13], -v[6:7]
	v_cvt_f32_f64_e32 v8, v[6:7]
	v_cvt_pk_bf16_f32 v8, v8, v4
	s_nop 0
	v_lshlrev_b32_e32 v10, 16, v8
	v_and_b32_e32 v14, 0xffff, v8
	v_cvt_f64_f32_e32 v[8:9], v10
	v_add_f64 v[6:7], v[6:7], -v[8:9]
	v_cvt_f32_f64_e32 v6, v[6:7]
	v_cvt_pk_bf16_f32 v15, v6, v4
	v_mov_b64_e32 v[8:9], s[2:3]
	v_and_or_b32 v1, v1, s1, v10
	v_and_or_b32 v10, v15, s1, 1.0
	v_mov_b64_e32 v[6:7], s[0:1]
	v_mov_b32_e32 v7, v10
	v_or_b32_e32 v10, 0xe0, v2
	v_mov_b32_e32 v6, v1
	v_lshl_add_u64 v[12:13], s[10:11], 0, v[10:11]
	global_store_dwordx4 v[12:13], v[6:9], off
	v_xor_b32_e32 v1, 0x80003f80, v5
	v_lshlrev_b32_e32 v5, 16, v15
	v_mov_b64_e32 v[8:9], s[2:3]
	v_bitop3_b32 v5, v5, s6, v14 bitop3:0x36
	v_mov_b64_e32 v[6:7], s[0:1]
	v_mov_b32_e32 v7, v1
	v_mov_b32_e32 v8, v5
	v_lshl_add_u64 v[10:11], s[8:9], 0, v[10:11]
	global_store_dwordx4 v[10:11], v[6:9], off
	v_or_b32_e32 v2, 0xf0, v2
	s_nop 0
	v_mul_f64 v[6:7], v[20:21], s[12:13]
	v_cvt_f32_f64_e32 v1, v[6:7]
	v_cvt_pk_bf16_f32 v1, v1, v4
	s_nop 0
	v_lshlrev_b32_e32 v10, 16, v1
	v_cvt_f64_f32_e32 v[6:7], v10
	v_fma_f64 v[6:7], v[20:21], s[12:13], -v[6:7]
	v_cvt_f32_f64_e32 v5, v[6:7]
	v_cvt_pk_bf16_f32 v5, v5, v4
	s_nop 0
	v_and_b32_e32 v11, 0xffff, v5
	v_lshlrev_b32_e32 v5, 16, v5
	v_cvt_f64_f32_e32 v[8:9], v5
	v_add_f64 v[6:7], v[6:7], -v[8:9]
	v_cvt_f32_f64_e32 v6, v[6:7]
	v_cvt_pk_bf16_f32 v12, v6, v4
	v_and_or_b32 v1, v1, s1, v5
	v_mov_b64_e32 v[6:7], s[2:3]
	v_and_or_b32 v8, v12, s1, 1.0
	v_mov_b64_e32 v[4:5], s[0:1]
	v_mov_b32_e32 v4, v1
	v_mov_b32_e32 v5, v8
	v_lshl_add_u64 v[8:9], s[10:11], 0, v[2:3]
	global_store_dwordx4 v[8:9], v[4:7], off
	v_xor_b32_e32 v1, 0x80003f80, v10
	v_lshl_add_u64 v[2:3], s[8:9], 0, v[2:3]
	v_lshlrev_b32_e32 v4, 16, v12
	v_bitop3_b32 v8, v4, s6, v11 bitop3:0x36
	v_mov_b64_e32 v[6:7], s[2:3]
	v_mov_b64_e32 v[4:5], s[0:1]
	v_mov_b32_e32 v5, v1
	v_mov_b32_e32 v6, v8
	v_readlane_b32 s1, v241, 3
	global_store_dwordx4 v[2:3], v[4:7], off
	s_barrier
	s_nop 0
	s_nop 0
	s_nop 0
	s_nop 0
	s_nop 0
	s_nop 0
	s_nop 0
	s_nop 0
